# P10 schedule tables: reuse the gate-up phase's LDS tables (ucum doubled) instead of re-loading counters and re-running the serial scan
# baseline (speedup 1.0000x reference)
.LBB0_958:
	s_cmp_lt_i32 s56, 11
	s_cselect_b64 s[0:1], -1, 0
	s_cmp_gt_i32 s57, 10
	s_cselect_b64 s[4:5], -1, 0
	s_and_b64 s[0:1], s[0:1], s[4:5]
	s_add_u32 s78, s46, 0xf500000
	s_addc_u32 s79, s47, 0
	s_andn2_b64 vcc, exec, s[0:1]
	s_cbranch_vccnz .LBB0_1069
	s_waitcnt vmcnt(0)
	v_mov_b32_e32 v2, v0
	s_waitcnt lgkmcnt(0)
	v_cmp_gt_i32_e32 vcc, 64, v2
	v_lshl_add_u32 v1, v2, 2, 0
	s_barrier
	s_movk_i32 s0, 0x42
	v_cmp_gt_i32_e32 vcc, s0, v2
	s_and_saveexec_b64 s[0:1], vcc
	s_cbranch_execz .LBB0_965
	v_add_u32_e32 v4, 0x20200, v1
	ds_read_b32 v3, v4
	s_waitcnt lgkmcnt(0)
	v_lshlrev_b32_e32 v3, 1, v3
	ds_write_b32 v4, v3
